# attention: first-tile slot DMA issue spread into the following QK segment (K after 3rd, V after 6th MFMA)
# speedup vs baseline: 1.0188x; 1.0105x over previous
; __device__ __forceinline__ void finishSM(f32x16& p0, f32x16& p1, float alpha, float& l_reg, bf16x8& pa0, bf16x8& pa1, bf16x8& pa2, bf16x8& pa3) {
;   for (int r = 0; r < 16; ++r) p1[r] = __builtin_amdgcn_exp2f(p1[r]);
;   float ps = 0; for (int r = 0; r < 16; ++r) ps += p0[r]; for (int r = 0; r < 16; ++r) ps += p1[r];
;   { auto rr = __builtin_amdgcn_permlane32_swap(__float_as_uint(ps), __float_as_uint(ps), false, false);
;     ps = __uint_as_float(rr[0]) + __uint_as_float(rr[1]); }
;   l_reg = l_reg * alpha + ps;
;     ...
;   PK4(p0, 0, pa0); PK4(p0, 8, pa1); PK4(p1, 0, pa2); PK4(p1, 8, pa3);
; template <bool HALF> __device__ __forceinline__ void qkt(f32x16& p0, f32x16& p1, const char* Ks, const bf16x8* qr, int r32, int hi, int koff) {
;   p0 = f32x16{}; p1 = f32x16{};
;   for (int d0 = 0; d0 < (HALF ? 4 : 8); ++d0) { int cb = (d0 * 16 + hi * 8) * 2 + koff;
;     bf16x8 b0 = *reinterpret_cast<const bf16x8*>(Ks + KSWZ(r32, cb));
;     bf16x8 b1 = *reinterpret_cast<const bf16x8*>(Ks + KSWZ(32 + r32, cb));
;     p0 = __builtin_amdgcn_mfma_f32_32x32x16_bf16(b0, qr[d0], p0, 0, 0, 0);
;     p1 = __builtin_amdgcn_mfma_f32_32x32x16_bf16(b1, qr[d0], p1, 0, 0, 0); }
.LBB0_425:
	ds_read_b128 v[64:67], v209 offset:49152
	ds_read_b128 v[68:71], v209 offset:57344
	ds_read_b128 v[190:193], v221 offset:49152
	ds_read_b128 v[228:231], v221 offset:57344
	v_add_f32_e32 v162, 0, v163
	v_add_f32_e32 v162, v177, v162
	s_waitcnt lgkmcnt(3)
	v_mfma_f32_32x32x16_bf16 v[80:95], v[64:67], v[118:121], 0
	v_add_f32_e32 v162, v164, v162
	v_add_f32_e32 v162, v188, v162
	v_add_f32_e32 v162, v176, v162
	v_add_f32_e32 v162, v189, v162
	v_add_f32_e32 v162, v165, v162
	v_add_f32_e32 v162, v175, v162
	v_add_f32_e32 v162, v166, v162
	s_waitcnt lgkmcnt(2)
	v_mfma_f32_32x32x16_bf16 v[64:79], v[68:71], v[118:121], 0
	v_add_f32_e32 v162, v173, v162
	v_add_f32_e32 v162, v167, v162
	v_add_f32_e32 v162, v174, v162
	v_exp_f32_e32 v160, v160
	v_add_f32_e32 v162, v168, v162
	v_exp_f32_e32 v161, v161
	v_add_f32_e32 v162, v171, v162
	s_waitcnt lgkmcnt(1)
	v_mfma_f32_32x32x16_bf16 v[80:95], v[190:193], v[126:129], v[80:95]
	v_exp_f32_e32 v158, v158
	v_add_f32_e32 v162, v169, v162
	v_exp_f32_e32 v159, v159
	v_add_f32_e32 v162, v172, v162
	v_exp_f32_e32 v154, v154
	v_add_f32_e32 v162, v160, v162
	v_exp_f32_e32 v155, v155
	s_waitcnt lgkmcnt(0)
	v_mfma_f32_32x32x16_bf16 v[64:79], v[228:231], v[126:129], v[64:79]
	ds_read_b128 v[190:193], v222 offset:49152
	ds_read_b128 v[228:231], v222 offset:57344
	v_add_f32_e32 v162, v161, v162
	v_exp_f32_e32 v150, v150
	v_add_f32_e32 v162, v158, v162
	v_exp_f32_e32 v151, v151
	v_add_f32_e32 v162, v159, v162
	v_exp_f32_e32 v148, v148
	s_waitcnt lgkmcnt(1)
	v_mfma_f32_32x32x16_bf16 v[80:95], v[190:193], v[122:125], v[80:95]
	v_add_f32_e32 v162, v154, v162
	v_exp_f32_e32 v149, v149
	v_add_f32_e32 v162, v155, v162
	v_exp_f32_e32 v156, v156
	v_add_f32_e32 v162, v150, v162
	v_exp_f32_e32 v157, v157
	v_add_f32_e32 v162, v151, v162
	s_waitcnt lgkmcnt(0)
	v_mfma_f32_32x32x16_bf16 v[64:79], v[228:231], v[122:125], v[64:79]
	ds_read_b128 v[190:193], v210 offset:49152
	ds_read_b128 v[228:231], v210 offset:57344
	v_exp_f32_e32 v152, v152
	v_add_f32_e32 v162, v148, v162
	v_exp_f32_e32 v153, v153
	v_add_f32_e32 v162, v149, v162
	v_exp_f32_e32 v146, v146
	v_add_f32_e32 v162, v156, v162
	s_waitcnt lgkmcnt(1)
	v_mfma_f32_32x32x16_bf16 v[80:95], v[190:193], v[114:117], v[80:95]
	v_exp_f32_e32 v147, v147
	v_add_f32_e32 v162, v157, v162
	v_add_f32_e32 v162, v152, v162
	v_add_f32_e32 v162, v153, v162
	v_add_f32_e32 v162, v146, v162
	v_add_f32_e32 v227, v147, v162
	s_waitcnt lgkmcnt(0)
	v_mfma_f32_32x32x16_bf16 v[64:79], v[228:231], v[114:117], v[64:79]
	ds_read_b128 v[190:193], v211 offset:49152
	ds_read_b128 v[228:231], v211 offset:57344
	s_waitcnt lgkmcnt(1)
	v_mfma_f32_32x32x16_bf16 v[80:95], v[190:193], v[110:113], v[80:95]
	s_waitcnt lgkmcnt(0)
	v_mfma_f32_32x32x16_bf16 v[64:79], v[228:231], v[110:113], v[64:79]
	ds_read_b128 v[190:193], v223 offset:49152
	ds_read_b128 v[228:231], v223 offset:57344
	s_waitcnt lgkmcnt(1)
	v_mfma_f32_32x32x16_bf16 v[80:95], v[190:193], v[106:109], v[80:95]
	s_waitcnt lgkmcnt(0)
	v_mfma_f32_32x32x16_bf16 v[64:79], v[228:231], v[106:109], v[64:79]
	ds_read_b128 v[190:193], v225 offset:49152
	ds_read_b128 v[228:231], v225 offset:57344
	s_waitcnt lgkmcnt(1)
	v_mfma_f32_32x32x16_bf16 v[80:95], v[190:193], v[102:105], v[80:95]
	s_waitcnt lgkmcnt(0)
	v_mfma_f32_32x32x16_bf16 v[64:79], v[228:231], v[102:105], v[64:79]
	ds_read_b128 v[190:193], v224 offset:49152
	ds_read_b128 v[228:231], v224 offset:57344
	v_cvt_pk_bf16_f32 v162, v163, v177
	v_cvt_pk_bf16_f32 v163, v164, v188
	v_cvt_pk_bf16_f32 v164, v176, v189
	v_cvt_pk_bf16_f32 v165, v165, v175
	v_cvt_pk_bf16_f32 v166, v166, v173
	v_cvt_pk_bf16_f32 v167, v167, v174
	s_waitcnt lgkmcnt(1)
	v_mfma_f32_32x32x16_bf16 v[80:95], v[190:193], v[98:101], v[80:95]
	v_permlane32_swap_b32_e32 v162, v164
	v_cvt_pk_bf16_f32 v168, v168, v171
	v_cvt_pk_bf16_f32 v169, v169, v172
	v_cvt_pk_bf16_f32 v172, v160, v161
	v_cvt_pk_bf16_f32 v173, v158, v159
	v_cvt_pk_bf16_f32 v174, v154, v155
	s_waitcnt lgkmcnt(0)
	v_mfma_f32_32x32x16_bf16 v[64:79], v[228:231], v[98:101], v[64:79]
	v_mov_b32_e32 v228, v227
	s_nop 1
	v_permlane32_swap_b32_e32 v227, v228
	v_cvt_pk_bf16_f32 v175, v150, v151
	v_cvt_pk_bf16_f32 v230, v148, v149
	v_cvt_pk_bf16_f32 v231, v156, v157
	v_cvt_pk_bf16_f32 v232, v152, v153
	v_cvt_pk_bf16_f32 v233, v146, v147
	v_permlane32_swap_b32_e32 v163, v165
	v_permlane32_swap_b32_e32 v166, v168
	v_permlane32_swap_b32_e32 v167, v169
	v_permlane32_swap_b32_e32 v172, v174
	v_permlane32_swap_b32_e32 v173, v175
	v_permlane32_swap_b32_e32 v230, v232
	v_permlane32_swap_b32_e32 v231, v233
	ds_read_b64_tr_b16 v[234:235], v204 offset:0
	ds_read_b64_tr_b16 v[236:237], v204 offset:0x800
	ds_read_b64_tr_b16 v[238:239], v204 offset:0x1000
	ds_read_b64_tr_b16 v[240:241], v204 offset:0x1800
	ds_read_b64_tr_b16 v[242:243], v204 offset:0x2000
	ds_read_b64_tr_b16 v[244:245], v204 offset:0x2800
	ds_read_b64_tr_b16 v[246:247], v204 offset:0x3000
	ds_read_b64_tr_b16 v[248:249], v204 offset:0x3800
	s_waitcnt lgkmcnt(0)
	s_nop 0
	v_mfma_f32_32x32x16_bf16 v[0:15], v[162:165], v[234:237], v[0:15]
	ds_read_b64_tr_b16 v[234:235], v204 offset:0x200
	ds_read_b64_tr_b16 v[236:237], v204 offset:0xa00
	v_mfma_f32_32x32x16_bf16 v[0:15], v[166:169], v[238:241], v[0:15]
	ds_read_b64_tr_b16 v[238:239], v204 offset:0x1200
	ds_read_b64_tr_b16 v[240:241], v204 offset:0x1a00
	v_mfma_f32_32x32x16_bf16 v[0:15], v[172:175], v[242:245], v[0:15]
	ds_read_b64_tr_b16 v[242:243], v204 offset:0x2200
	ds_read_b64_tr_b16 v[244:245], v204 offset:0x2a00
	v_mfma_f32_32x32x16_bf16 v[0:15], v[230:233], v[246:249], v[0:15]
	ds_read_b64_tr_b16 v[246:247], v204 offset:0x3200
	ds_read_b64_tr_b16 v[248:249], v204 offset:0x3a00
	s_waitcnt lgkmcnt(0)
; #define SBAR() __builtin_amdgcn_sched_barrier(0)
; __device__ __forceinline__ void partialSM(f32x16& p0, f32x16& p1, float& m_reg, float& mn, float& alpha) {
;     ...
;   float pmax = p0[0]; for (int r = 1; r < 16; ++r) pmax = fmaxf(pmax, p0[r]); for (int r = 0; r < 16; ++r) pmax = fmaxf(pmax, p1[r]);
;   { auto rr = __builtin_amdgcn_permlane32_swap(__float_as_uint(pmax), __float_as_uint(pmax), false, false);
;     pmax = fmaxf(__uint_as_float(rr[0]), __uint_as_float(rr[1])); }
;   if (__builtin_expect(__all(pmax - m_reg <= THR / SCALE), 1)) { mn = m_reg; alpha = 1.f; }
;   else { mn = fmaxf(m_reg, pmax); alpha = __builtin_amdgcn_exp2f((m_reg - mn) * C); m_reg = mn; }
; template <int D0> __device__ __forceinline__ void pv_one(f32x16& od, int vb, bf16x8 pa0, bf16x8 pa1, bf16x8 pa2, bf16x8 pa3) {
;   const s16x4 l0 = tr_read<v_rd_off(D0, 0, 0)>(vb), h0 = tr_read<v_rd_off(D0, 0, 1)>(vb), l1 = tr_read<v_rd_off(D0, 1, 0)>(vb), h1 = tr_read<v_rd_off(D0, 1, 1)>(vb);
;   const s16x4 l2 = tr_read<v_rd_off(D0, 2, 0)>(vb), h2 = tr_read<v_rd_off(D0, 2, 1)>(vb), l3 = tr_read<v_rd_off(D0, 3, 0)>(vb), h3 = tr_read<v_rd_off(D0, 3, 1)>(vb);
;   asm volatile("s_waitcnt lgkmcnt(0)" ::: "memory"); SBAR();
;     ...
;   od = __builtin_amdgcn_mfma_f32_32x32x16_bf16(pa0, PK(l0, h0), od, 0, 0, 0);
;   od = __builtin_amdgcn_mfma_f32_32x32x16_bf16(pa1, PK(l1, h1), od, 0, 0, 0);
;   od = __builtin_amdgcn_mfma_f32_32x32x16_bf16(pa2, PK(l2, h2), od, 0, 0, 0);
;   od = __builtin_amdgcn_mfma_f32_32x32x16_bf16(pa3, PK(l3, h3), od, 0, 0, 0);
;     ...
; }
; __device__ __forceinline__ void pv_d0(f32x16* o, int vb, bf16x8 pa0, bf16x8 pa1, bf16x8 pa2, bf16x8 pa3) {
;   pv_one<0>(o[0], vb, pa0, pa1, pa2, pa3); pv_one<1>(o[1], vb, pa0, pa1, pa2, pa3); pv_one<2>(o[2], vb, pa0, pa1, pa2, pa3); pv_one<3>(o[3], vb, pa0, pa1, pa2, pa3);
	v_mfma_f32_32x32x16_bf16 v[48:63], v[162:165], v[234:237], v[48:63]
	ds_read_b64_tr_b16 v[234:235], v204 offset:0x400
	ds_read_b64_tr_b16 v[236:237], v204 offset:0xc00
	v_mfma_f32_32x32x16_bf16 v[48:63], v[166:169], v[238:241], v[48:63]
	ds_read_b64_tr_b16 v[238:239], v204 offset:0x1400
	ds_read_b64_tr_b16 v[240:241], v204 offset:0x1c00
	v_mfma_f32_32x32x16_bf16 v[48:63], v[172:175], v[242:245], v[48:63]
	ds_read_b64_tr_b16 v[242:243], v204 offset:0x2400
	ds_read_b64_tr_b16 v[244:245], v204 offset:0x2c00
	v_mfma_f32_32x32x16_bf16 v[48:63], v[230:233], v[246:249], v[48:63]
	ds_read_b64_tr_b16 v[246:247], v204 offset:0x3400
	ds_read_b64_tr_b16 v[248:249], v204 offset:0x3c00
	s_waitcnt lgkmcnt(0)
	v_mfma_f32_32x32x16_bf16 v[32:47], v[162:165], v[234:237], v[32:47]
	ds_read_b64_tr_b16 v[234:235], v204 offset:0x600
	ds_read_b64_tr_b16 v[236:237], v204 offset:0xe00
	v_mfma_f32_32x32x16_bf16 v[32:47], v[166:169], v[238:241], v[32:47]
	ds_read_b64_tr_b16 v[238:239], v204 offset:0x1600
	ds_read_b64_tr_b16 v[240:241], v204 offset:0x1e00
	v_mfma_f32_32x32x16_bf16 v[32:47], v[172:175], v[242:245], v[32:47]
	ds_read_b64_tr_b16 v[242:243], v204 offset:0x2600
	ds_read_b64_tr_b16 v[244:245], v204 offset:0x2e00
	v_mfma_f32_32x32x16_bf16 v[32:47], v[230:233], v[246:249], v[32:47]
	ds_read_b64_tr_b16 v[246:247], v204 offset:0x3600
	ds_read_b64_tr_b16 v[248:249], v204 offset:0x3e00
	s_waitcnt lgkmcnt(0)
	v_mfma_f32_32x32x16_bf16 v[16:31], v[162:165], v[234:237], v[16:31]
	v_max_f32_e32 v162, v81, v81
	v_max_f32_e32 v163, v80, v80
	v_max_f32_e32 v162, v163, v162
	v_max3_f32 v162, v162, v82, v83
	v_max3_f32 v162, v162, v84, v85
	v_max3_f32 v162, v162, v86, v87
	v_max3_f32 v162, v162, v88, v89
	v_max3_f32 v162, v162, v90, v91
	v_max3_f32 v162, v162, v92, v93
	v_mfma_f32_32x32x16_bf16 v[16:31], v[166:169], v[238:241], v[16:31]
	v_max3_f32 v162, v162, v94, v95
	v_max3_f32 v162, v162, v64, v65
	v_max3_f32 v162, v162, v66, v67
	v_max3_f32 v162, v162, v68, v69
	v_max3_f32 v162, v162, v70, v71
	v_max3_f32 v162, v162, v72, v73
	v_max3_f32 v162, v162, v74, v75
	v_max3_f32 v162, v162, v76, v77
	v_mfma_f32_32x32x16_bf16 v[16:31], v[172:175], v[242:245], v[16:31]
	v_max3_f32 v162, v162, v78, v79
	v_mov_b32_e32 v163, v162
	s_nop 1
	v_permlane32_swap_b32_e32 v162, v163
	v_max_f32_e32 v163, v163, v163
	v_max_f32_e32 v162, v162, v162
	v_max_f32_e32 v162, v162, v163
	v_sub_f32_e32 v163, v162, v170
	v_cmp_ge_f32_e32 vcc, s87, v163
	v_max_f32_e32 v163, v170, v170
	v_max_f32_e32 v162, v163, v162
	v_mfma_f32_32x32x16_bf16 v[16:31], v[230:233], v[246:249], v[16:31]
	v_sub_f32_e32 v163, v170, v162
	v_mul_f32_e32 v163, 0x3e0293ee, v163
	v_exp_f32_e32 v163, v163
	s_cmp_eq_u64 vcc, exec
	s_cselect_b64 s[42:43], -1, 0
	s_waitcnt vmcnt(0)
	s_barrier
	v_cndmask_b32_e64 v229, v163, 1.0, s[42:43]
	v_cmp_gt_f32_e32 vcc, 1.0, v229
	s_cbranch_vccz .LBB0_429
	s_and_saveexec_b64 s[6:7], s[40:41]
	ds_write_b32 v201, v229 offset:128
	s_or_b64 exec, exec, s[6:7]
	s_waitcnt lgkmcnt(0)
	v_add_u32_e32 v163, v200, v96
	ds_read_b128 v[164:167], v163 offset:224
	ds_read_b128 v[172:175], v163 offset:192
	ds_read_b128 v[230:233], v163 offset:160
	ds_read_b128 v[234:237], v163 offset:128
	s_waitcnt lgkmcnt(3)
	v_pk_mul_f32 v[12:13], v[12:13], v[164:165]
	s_waitcnt lgkmcnt(2)
	v_pk_mul_f32 v[8:9], v[8:9], v[172:173]
	s_waitcnt lgkmcnt(1)
	v_pk_mul_f32 v[4:5], v[4:5], v[230:231]
	v_pk_mul_f32 v[14:15], v[14:15], v[166:167]
	v_pk_mul_f32 v[10:11], v[10:11], v[174:175]
	v_pk_mul_f32 v[6:7], v[6:7], v[232:233]
	s_waitcnt lgkmcnt(0)
	v_pk_mul_f32 v[2:3], v[2:3], v[236:237]
	v_pk_mul_f32 v[0:1], v[0:1], v[234:235]
	v_pk_mul_f32 v[60:61], v[60:61], v[164:165]
	v_pk_mul_f32 v[56:57], v[56:57], v[172:173]
	v_pk_mul_f32 v[52:53], v[52:53], v[230:231]
	v_pk_mul_f32 v[62:63], v[62:63], v[166:167]
	v_pk_mul_f32 v[58:59], v[58:59], v[174:175]
	v_pk_mul_f32 v[54:55], v[54:55], v[232:233]
	v_pk_mul_f32 v[50:51], v[50:51], v[236:237]
	v_pk_mul_f32 v[48:49], v[48:49], v[234:235]
	v_pk_mul_f32 v[44:45], v[44:45], v[164:165]
	v_pk_mul_f32 v[40:41], v[40:41], v[172:173]
	v_pk_mul_f32 v[36:37], v[36:37], v[230:231]
	v_pk_mul_f32 v[46:47], v[46:47], v[166:167]
	v_pk_mul_f32 v[42:43], v[42:43], v[174:175]
	v_pk_mul_f32 v[38:39], v[38:39], v[232:233]
	v_pk_mul_f32 v[34:35], v[34:35], v[236:237]
	v_pk_mul_f32 v[32:33], v[32:33], v[234:235]
	v_pk_mul_f32 v[28:29], v[28:29], v[164:165]
	v_pk_mul_f32 v[24:25], v[24:25], v[172:173]
	v_pk_mul_f32 v[20:21], v[20:21], v[230:231]
	v_pk_mul_f32 v[30:31], v[30:31], v[166:167]
	v_pk_mul_f32 v[26:27], v[26:27], v[174:175]
	v_pk_mul_f32 v[22:23], v[22:23], v[232:233]
	v_pk_mul_f32 v[18:19], v[18:19], v[236:237]
	v_pk_mul_f32 v[16:17], v[16:17], v[234:235]
; __device__ __forceinline__ void partialSM(f32x16& p0, f32x16& p1, float& m_reg, float& mn, float& alpha) {
;     ...
;   float mnC = -mn * C;
;   for (int r = 0; r < 16; ++r) p0[r] = fmaf(p0[r], C, mnC); for (int r = 0; r < 16; ++r) p1[r] = fmaf(p1[r], C, mnC);
;   for (int r = 0; r < 16; ++r) p0[r] = __builtin_amdgcn_exp2f(p0[r]);
; }
; __device__ __forceinline__ void finishSM(f32x16& p0, f32x16& p1, float alpha, float& l_reg, bf16x8& pa0, bf16x8& pa1, bf16x8& pa2, bf16x8& pa3) {
;   for (int r = 0; r < 16; ++r) p1[r] = __builtin_amdgcn_exp2f(p1[r]);
;   float ps = 0; for (int r = 0; r < 16; ++r) ps += p0[r]; for (int r = 0; r < 16; ++r) ps += p1[r];
;   { auto rr = __builtin_amdgcn_permlane32_swap(__float_as_uint(ps), __float_as_uint(ps), false, false);
;     ps = __uint_as_float(rr[0]) + __uint_as_float(rr[1]); }
;   l_reg = l_reg * alpha + ps;
;     ...
;   PK4(p0, 0, pa0); PK4(p0, 8, pa1); PK4(p1, 0, pa2); PK4(p1, 8, pa3);
;     ...
; }
; template <bool HALF> __device__ __forceinline__ void qkt(f32x16& p0, f32x16& p1, const char* Ks, const bf16x8* qr, int r32, int hi, int koff) {
;   p0 = f32x16{}; p1 = f32x16{};
;   for (int d0 = 0; d0 < (HALF ? 4 : 8); ++d0) { int cb = (d0 * 16 + hi * 8) * 2 + koff;
;     bf16x8 b0 = *reinterpret_cast<const bf16x8*>(Ks + KSWZ(r32, cb));
;     bf16x8 b1 = *reinterpret_cast<const bf16x8*>(Ks + KSWZ(32 + r32, cb));
;     p0 = __builtin_amdgcn_mfma_f32_32x32x16_bf16(b0, qr[d0], p0, 0, 0, 0);
;     p1 = __builtin_amdgcn_mfma_f32_32x32x16_bf16(b1, qr[d0], p1, 0, 0, 0); }
.LBB0_429:
	v_cndmask_b32_e64 v230, v162, v170, s[42:43]
	v_mul_f32_e32 v231, 0xbe0293ee, v230
	v_fmamk_f32 v80, v80, 0x3e0293ee, v231
	v_fmamk_f32 v81, v81, 0x3e0293ee, v231
	v_fmamk_f32 v82, v82, 0x3e0293ee, v231
	v_fmamk_f32 v83, v83, 0x3e0293ee, v231
	v_fmamk_f32 v84, v84, 0x3e0293ee, v231
	v_fmamk_f32 v85, v85, 0x3e0293ee, v231
	v_fmamk_f32 v86, v86, 0x3e0293ee, v231
	v_fmamk_f32 v87, v87, 0x3e0293ee, v231
	v_fmamk_f32 v88, v88, 0x3e0293ee, v231
	v_fmamk_f32 v89, v89, 0x3e0293ee, v231
	v_fmamk_f32 v90, v90, 0x3e0293ee, v231
	v_fmamk_f32 v91, v91, 0x3e0293ee, v231
	v_fmamk_f32 v92, v92, 0x3e0293ee, v231
	v_fmamk_f32 v93, v93, 0x3e0293ee, v231
	v_fmamk_f32 v94, v94, 0x3e0293ee, v231
	v_fmamk_f32 v95, v95, 0x3e0293ee, v231
	v_exp_f32_e32 v162, v80
	v_exp_f32_e32 v177, v81
	v_exp_f32_e32 v163, v82
	v_exp_f32_e32 v176, v83
	v_exp_f32_e32 v164, v84
	v_exp_f32_e32 v175, v85
	v_exp_f32_e32 v165, v86
	v_exp_f32_e32 v174, v87
	v_exp_f32_e32 v166, v88
	v_exp_f32_e32 v173, v89
	v_exp_f32_e32 v167, v90
	v_exp_f32_e32 v172, v91
	v_exp_f32_e32 v168, v92
	v_exp_f32_e32 v171, v93
	v_exp_f32_e32 v169, v94
	v_exp_f32_e32 v170, v95
	v_fmamk_f32 v240, v64, 0x3e0293ee, v231
	v_fmamk_f32 v241, v65, 0x3e0293ee, v231
	v_fmamk_f32 v242, v66, 0x3e0293ee, v231
	v_fmamk_f32 v243, v67, 0x3e0293ee, v231
	v_fmamk_f32 v244, v68, 0x3e0293ee, v231
	v_fmamk_f32 v233, v69, 0x3e0293ee, v231
	v_fmamk_f32 v234, v70, 0x3e0293ee, v231
	v_fmamk_f32 v235, v71, 0x3e0293ee, v231
	v_fmamk_f32 v236, v72, 0x3e0293ee, v231
	v_fmamk_f32 v237, v73, 0x3e0293ee, v231
	v_fmamk_f32 v238, v74, 0x3e0293ee, v231
	v_fmamk_f32 v239, v75, 0x3e0293ee, v231
	v_fmamk_f32 v232, v76, 0x3e0293ee, v231
	v_fmamk_f32 v245, v77, 0x3e0293ee, v231
	v_fmamk_f32 v246, v78, 0x3e0293ee, v231
	v_fmac_f32_e32 v231, 0x3e0293ee, v79
	s_waitcnt lgkmcnt(0)
	ds_read_b128 v[64:67], v209 offset:32768
	ds_read_b128 v[68:71], v209 offset:40960
	ds_read_b128 v[248:251], v221 offset:32768
	ds_read_b128 v[212:215], v221 offset:40960
	v_exp_f32_e32 v233, v233
	v_exp_f32_e32 v234, v234
	s_waitcnt lgkmcnt(3)
	v_mfma_f32_32x32x16_bf16 v[80:95], v[64:67], v[118:121], 0
	v_exp_f32_e32 v235, v235
	v_exp_f32_e32 v236, v236
	v_exp_f32_e32 v237, v237
	v_exp_f32_e32 v238, v238
	v_exp_f32_e32 v239, v239
	s_waitcnt lgkmcnt(2)
	v_mfma_f32_32x32x16_bf16 v[64:79], v[68:71], v[118:121], 0
	s_waitcnt lgkmcnt(1)
	v_mfma_f32_32x32x16_bf16 v[80:95], v[248:251], v[126:129], v[80:95]
	s_add_i32 m0, s52, 0x4000
	s_nop 0
	global_load_lds_dwordx4 v130, s[48:49]
	s_add_i32 m0, s52, 0x4400
	s_nop 0
	global_load_lds_dwordx4 v131, s[48:49]
	s_add_u32 s48, s48, 0x18000
	s_addc_u32 s49, s49, 0
	s_waitcnt lgkmcnt(0)
	v_mfma_f32_32x32x16_bf16 v[64:79], v[212:215], v[126:129], v[64:79]
	ds_read_b128 v[212:215], v222 offset:32768
	ds_read_b128 v[248:251], v222 offset:40960
	s_waitcnt lgkmcnt(1)
	v_mfma_f32_32x32x16_bf16 v[80:95], v[212:215], v[122:125], v[80:95]
	s_waitcnt lgkmcnt(0)
	v_mfma_f32_32x32x16_bf16 v[64:79], v[248:251], v[122:125], v[64:79]
	s_add_i32 m0, s53, 0x0
	s_nop 0
	global_load_lds_dwordx4 v132, s[50:51]
	s_add_i32 m0, s53, 0x400
	s_nop 0
	global_load_lds_dwordx4 v133, s[50:51]
	s_add_u32 s50, s50, 0xc0000
	s_addc_u32 s51, s51, 0
	ds_read_b128 v[212:215], v210 offset:32768
	ds_read_b128 v[248:251], v210 offset:40960
	s_waitcnt lgkmcnt(1)
	v_mfma_f32_32x32x16_bf16 v[80:95], v[212:215], v[114:117], v[80:95]
	s_waitcnt lgkmcnt(0)
	v_mfma_f32_32x32x16_bf16 v[64:79], v[248:251], v[114:117], v[64:79]
	ds_read_b128 v[212:215], v211 offset:32768
	ds_read_b128 v[248:251], v211 offset:40960
	s_waitcnt lgkmcnt(1)
	v_mfma_f32_32x32x16_bf16 v[80:95], v[212:215], v[110:113], v[80:95]
	s_waitcnt lgkmcnt(0)
	v_mfma_f32_32x32x16_bf16 v[64:79], v[248:251], v[110:113], v[64:79]
	ds_read_b128 v[212:215], v223 offset:32768
	ds_read_b128 v[248:251], v223 offset:40960
	s_waitcnt lgkmcnt(1)
	v_mfma_f32_32x32x16_bf16 v[80:95], v[212:215], v[106:109], v[80:95]
	s_waitcnt lgkmcnt(0)
	v_mfma_f32_32x32x16_bf16 v[64:79], v[248:251], v[106:109], v[64:79]
	ds_read_b128 v[212:215], v225 offset:32768
	ds_read_b128 v[248:251], v225 offset:40960
	s_waitcnt lgkmcnt(1)
	v_mfma_f32_32x32x16_bf16 v[80:95], v[212:215], v[102:105], v[80:95]
	s_waitcnt lgkmcnt(0)
	v_mfma_f32_32x32x16_bf16 v[64:79], v[248:251], v[102:105], v[64:79]
	ds_read_b128 v[212:215], v224 offset:32768
	ds_read_b128 v[248:251], v224 offset:40960
	s_waitcnt lgkmcnt(1)
	v_mfma_f32_32x32x16_bf16 v[80:95], v[212:215], v[98:101], v[80:95]
	v_exp_f32_e32 v212, v240
	v_exp_f32_e32 v240, v244
	v_exp_f32_e32 v244, v231
	v_add_f32_e32 v231, 0, v162
	v_add_f32_e32 v231, v177, v231
	v_add_f32_e32 v231, v163, v231
	v_add_f32_e32 v231, v176, v231
	v_add_f32_e32 v231, v164, v231
	v_add_f32_e32 v231, v175, v231
	v_add_f32_e32 v231, v165, v231
	v_add_f32_e32 v231, v174, v231
	v_add_f32_e32 v231, v166, v231
	v_add_f32_e32 v231, v173, v231
	v_add_f32_e32 v231, v167, v231
	v_add_f32_e32 v231, v172, v231
	v_add_f32_e32 v231, v168, v231
	v_exp_f32_e32 v213, v241
	v_add_f32_e32 v231, v171, v231
	v_exp_f32_e32 v214, v242
	v_add_f32_e32 v231, v169, v231
	v_exp_f32_e32 v215, v243
	v_add_f32_e32 v231, v170, v231
	v_add_f32_e32 v231, v212, v231
	v_add_f32_e32 v231, v213, v231
	v_add_f32_e32 v231, v214, v231
	v_add_f32_e32 v231, v215, v231
	v_add_f32_e32 v231, v240, v231
	v_add_f32_e32 v231, v233, v231
	v_add_f32_e32 v231, v234, v231
	v_add_f32_e32 v231, v235, v231
	v_exp_f32_e32 v241, v232
	v_add_f32_e32 v231, v236, v231
	v_exp_f32_e32 v242, v245
	v_add_f32_e32 v231, v237, v231
	s_waitcnt lgkmcnt(0)
	v_mfma_f32_32x32x16_bf16 v[64:79], v[248:251], v[98:101], v[64:79]
	v_exp_f32_e32 v243, v246
	v_add_f32_e32 v231, v238, v231
	v_add_f32_e32 v231, v239, v231
	v_add_f32_e32 v231, v241, v231
	v_add_f32_e32 v231, v242, v231
	v_add_f32_e32 v231, v243, v231
	v_add_f32_e32 v231, v244, v231
	v_mov_b32_e32 v232, v231
	v_cvt_pk_bf16_f32 v162, v162, v177
	v_cvt_pk_bf16_f32 v163, v163, v176
	v_cvt_pk_bf16_f32 v164, v164, v175
	v_cvt_pk_bf16_f32 v165, v165, v174
	v_cvt_pk_bf16_f32 v166, v166, v173
	v_cvt_pk_bf16_f32 v167, v167, v172
	v_cvt_pk_bf16_f32 v168, v168, v171
	v_cvt_pk_bf16_f32 v169, v169, v170
	v_cvt_pk_bf16_f32 v170, v212, v213
	v_cvt_pk_bf16_f32 v171, v214, v215
	v_cvt_pk_bf16_f32 v172, v240, v233
	v_cvt_pk_bf16_f32 v173, v234, v235
	v_cvt_pk_bf16_f32 v174, v236, v237
	v_cvt_pk_bf16_f32 v175, v238, v239
	v_cvt_pk_bf16_f32 v176, v241, v242
	v_cvt_pk_bf16_f32 v177, v243, v244
	s_nop 1
	v_permlane32_swap_b32_e32 v231, v232
	v_permlane32_swap_b32_e32 v162, v164
	v_permlane32_swap_b32_e32 v163, v165
	v_permlane32_swap_b32_e32 v166, v168
	v_permlane32_swap_b32_e32 v167, v169
	v_permlane32_swap_b32_e32 v170, v172
	v_permlane32_swap_b32_e32 v171, v173
	v_permlane32_swap_b32_e32 v174, v176
	v_permlane32_swap_b32_e32 v175, v177
	s_cmp_ge_u32 s2, s4
	s_cselect_b64 s[20:21], -1, 0

; __device__ __forceinline__ void finishSM(f32x16& p0, f32x16& p1, float alpha, float& l_reg, bf16x8& pa0, bf16x8& pa1, bf16x8& pa2, bf16x8& pa3) {
;   for (int r = 0; r < 16; ++r) p1[r] = __builtin_amdgcn_exp2f(p1[r]);
;   float ps = 0; for (int r = 0; r < 16; ++r) ps += p0[r]; for (int r = 0; r < 16; ++r) ps += p1[r];
;   { auto rr = __builtin_amdgcn_permlane32_swap(__float_as_uint(ps), __float_as_uint(ps), false, false);
;     ps = __uint_as_float(rr[0]) + __uint_as_float(rr[1]); }
;   l_reg = l_reg * alpha + ps;
;     ...
;   PK4(p0, 0, pa0); PK4(p0, 8, pa1); PK4(p1, 0, pa2); PK4(p1, 8, pa3);
; template <bool HALF> __device__ __forceinline__ void qkt(f32x16& p0, f32x16& p1, const char* Ks, const bf16x8* qr, int r32, int hi, int koff) {
;   p0 = f32x16{}; p1 = f32x16{};
;   for (int d0 = 0; d0 < (HALF ? 4 : 8); ++d0) { int cb = (d0 * 16 + hi * 8) * 2 + koff;
;     bf16x8 b0 = *reinterpret_cast<const bf16x8*>(Ks + KSWZ(r32, cb));
;     bf16x8 b1 = *reinterpret_cast<const bf16x8*>(Ks + KSWZ(32 + r32, cb));
;     p0 = __builtin_amdgcn_mfma_f32_32x32x16_bf16(b0, qr[d0], p0, 0, 0, 0);
;     p1 = __builtin_amdgcn_mfma_f32_32x32x16_bf16(b1, qr[d0], p1, 0, 0, 0); }
.LBB0_454:
	ds_read_b128 v[64:67], v192 offset:49152
	ds_read_b128 v[68:71], v192 offset:57344
	v_add_f32_e32 v146, 0, v147
	v_add_f32_e32 v146, v160, v146
	v_add_f32_e32 v146, v148, v146
	s_waitcnt lgkmcnt(1)
	v_mfma_f32_32x32x16_bf16 v[80:95], v[64:67], v[98:101], 0
	v_add_f32_e32 v146, v161, v146
	v_add_f32_e32 v146, v149, v146
	ds_read_b128 v[172:175], v193 offset:49152
	ds_read_b128 v[198:201], v193 offset:57344
	v_add_f32_e32 v146, v170, v146
	v_add_f32_e32 v146, v159, v146
	v_add_f32_e32 v146, v171, v146
	v_add_f32_e32 v146, v151, v146
	s_waitcnt lgkmcnt(2)
	v_mfma_f32_32x32x16_bf16 v[64:79], v[68:71], v[98:101], 0
	v_add_f32_e32 v146, v155, v146
	v_add_f32_e32 v146, v152, v146
	v_add_f32_e32 v146, v156, v146
	v_exp_f32_e32 v144, v144
	v_add_f32_e32 v146, v153, v146
	v_exp_f32_e32 v145, v145
	v_add_f32_e32 v146, v157, v146
	s_waitcnt lgkmcnt(1)
	v_mfma_f32_32x32x16_bf16 v[80:95], v[172:175], v[106:109], v[80:95]
	v_exp_f32_e32 v142, v142
	v_add_f32_e32 v146, v154, v146
	v_exp_f32_e32 v143, v143
	v_add_f32_e32 v146, v158, v146
	v_exp_f32_e32 v138, v138
	v_add_f32_e32 v146, v144, v146
	v_exp_f32_e32 v139, v139
	s_waitcnt lgkmcnt(0)
	v_mfma_f32_32x32x16_bf16 v[64:79], v[198:201], v[106:109], v[64:79]
	ds_read_b128 v[172:175], v195 offset:49152
	ds_read_b128 v[198:201], v195 offset:57344
	v_add_f32_e32 v146, v145, v146
	v_exp_f32_e32 v134, v134
	v_add_f32_e32 v146, v142, v146
	v_exp_f32_e32 v135, v135
	v_add_f32_e32 v146, v143, v146
	v_exp_f32_e32 v132, v132
	s_waitcnt lgkmcnt(1)
	v_mfma_f32_32x32x16_bf16 v[80:95], v[172:175], v[110:113], v[80:95]
	v_add_f32_e32 v146, v138, v146
	v_exp_f32_e32 v133, v133
	v_add_f32_e32 v146, v139, v146
	v_exp_f32_e32 v140, v140
	v_add_f32_e32 v146, v134, v146
	v_exp_f32_e32 v141, v141
	v_add_f32_e32 v146, v135, v146
	s_waitcnt lgkmcnt(0)
	v_mfma_f32_32x32x16_bf16 v[64:79], v[198:201], v[110:113], v[64:79]
	ds_read_b128 v[172:175], v194 offset:49152
	ds_read_b128 v[198:201], v194 offset:57344
	v_exp_f32_e32 v136, v136
	v_add_f32_e32 v146, v132, v146
	v_exp_f32_e32 v137, v137
	v_add_f32_e32 v146, v133, v146
	v_exp_f32_e32 v130, v130
	v_add_f32_e32 v146, v140, v146
	s_waitcnt lgkmcnt(1)
	v_mfma_f32_32x32x16_bf16 v[80:95], v[172:175], v[102:105], v[80:95]
	v_exp_f32_e32 v131, v131
	v_add_f32_e32 v146, v141, v146
	v_add_f32_e32 v146, v136, v146
	v_add_f32_e32 v146, v137, v146
	v_add_f32_e32 v146, v130, v146
	s_waitcnt lgkmcnt(0)
	v_mfma_f32_32x32x16_bf16 v[64:79], v[198:201], v[102:105], v[64:79]
	v_add_f32_e32 v198, v131, v146
	v_mov_b32_e32 v199, v198
	v_cvt_pk_bf16_f32 v146, v147, v160
	v_cvt_pk_bf16_f32 v147, v148, v161
	v_cvt_pk_bf16_f32 v148, v149, v170
	v_cvt_pk_bf16_f32 v149, v159, v171
	v_cvt_pk_bf16_f32 v200, v151, v155
	v_cvt_pk_bf16_f32 v201, v152, v156
	v_cvt_pk_bf16_f32 v202, v153, v157
	s_nop 1
	v_permlane32_swap_b32_e32 v198, v199
	v_permlane32_swap_b32_e32 v146, v148
	v_cvt_pk_bf16_f32 v203, v154, v158
	v_permlane32_swap_b32_e32 v200, v202
	v_cvt_pk_bf16_f32 v152, v144, v145
	v_cvt_pk_bf16_f32 v153, v142, v143
	v_cvt_pk_bf16_f32 v154, v138, v139
	v_cvt_pk_bf16_f32 v155, v134, v135
	v_cvt_pk_bf16_f32 v156, v132, v133
	v_cvt_pk_bf16_f32 v157, v140, v141
	v_cvt_pk_bf16_f32 v158, v136, v137
	v_cvt_pk_bf16_f32 v159, v130, v131
	v_permlane32_swap_b32_e32 v147, v149
	v_permlane32_swap_b32_e32 v201, v203
	v_permlane32_swap_b32_e32 v152, v154
	v_permlane32_swap_b32_e32 v153, v155
	v_permlane32_swap_b32_e32 v156, v158
	v_permlane32_swap_b32_e32 v157, v159
	ds_read_b64_tr_b16 v[204:205], v187 offset:0
	ds_read_b64_tr_b16 v[206:207], v187 offset:0x800
	ds_read_b64_tr_b16 v[208:209], v187 offset:0x1000
	ds_read_b64_tr_b16 v[210:211], v187 offset:0x1800
	ds_read_b64_tr_b16 v[212:213], v187 offset:0x2000
	ds_read_b64_tr_b16 v[214:215], v187 offset:0x2800
	ds_read_b64_tr_b16 v[222:223], v187 offset:0x3000
	ds_read_b64_tr_b16 v[224:225], v187 offset:0x3800
	s_waitcnt lgkmcnt(0)
	s_nop 0
	v_mfma_f32_32x32x16_bf16 v[0:15], v[146:149], v[204:207], v[0:15]
	ds_read_b64_tr_b16 v[204:205], v187 offset:0x200
	ds_read_b64_tr_b16 v[206:207], v187 offset:0xa00
	v_mfma_f32_32x32x16_bf16 v[0:15], v[200:203], v[208:211], v[0:15]
	ds_read_b64_tr_b16 v[208:209], v187 offset:0x1200
	ds_read_b64_tr_b16 v[210:211], v187 offset:0x1a00
	v_mfma_f32_32x32x16_bf16 v[0:15], v[152:155], v[212:215], v[0:15]
	ds_read_b64_tr_b16 v[212:213], v187 offset:0x2200
	ds_read_b64_tr_b16 v[214:215], v187 offset:0x2a00
	v_mfma_f32_32x32x16_bf16 v[0:15], v[156:159], v[222:225], v[0:15]
	ds_read_b64_tr_b16 v[222:223], v187 offset:0x3200
	ds_read_b64_tr_b16 v[224:225], v187 offset:0x3a00
	s_waitcnt lgkmcnt(0)
	v_mfma_f32_32x32x16_bf16 v[48:63], v[146:149], v[204:207], v[48:63]
	ds_read_b64_tr_b16 v[204:205], v187 offset:0x400
	ds_read_b64_tr_b16 v[206:207], v187 offset:0xc00
	v_mfma_f32_32x32x16_bf16 v[48:63], v[200:203], v[208:211], v[48:63]
	ds_read_b64_tr_b16 v[208:209], v187 offset:0x1400
	ds_read_b64_tr_b16 v[210:211], v187 offset:0x1c00
	v_mfma_f32_32x32x16_bf16 v[48:63], v[152:155], v[212:215], v[48:63]
	ds_read_b64_tr_b16 v[212:213], v187 offset:0x2400
	ds_read_b64_tr_b16 v[214:215], v187 offset:0x2c00
	v_mfma_f32_32x32x16_bf16 v[48:63], v[156:159], v[222:225], v[48:63]
	ds_read_b64_tr_b16 v[222:223], v187 offset:0x3400
	ds_read_b64_tr_b16 v[224:225], v187 offset:0x3c00
	s_waitcnt lgkmcnt(0)
; #define SBAR() __builtin_amdgcn_sched_barrier(0)
; __device__ __forceinline__ void partialSM(f32x16& p0, f32x16& p1, float& m_reg, float& mn, float& alpha) {
;     ...
;   float pmax = p0[0]; for (int r = 1; r < 16; ++r) pmax = fmaxf(pmax, p0[r]); for (int r = 0; r < 16; ++r) pmax = fmaxf(pmax, p1[r]);
;   { auto rr = __builtin_amdgcn_permlane32_swap(__float_as_uint(pmax), __float_as_uint(pmax), false, false);
;     pmax = fmaxf(__uint_as_float(rr[0]), __uint_as_float(rr[1])); }
;   if (__builtin_expect(__all(pmax - m_reg <= THR / SCALE), 1)) { mn = m_reg; alpha = 1.f; }
;   else { mn = fmaxf(m_reg, pmax); alpha = __builtin_amdgcn_exp2f((m_reg - mn) * C); m_reg = mn; }
; template <int D0> __device__ __forceinline__ void pv_one(f32x16& od, int vb, bf16x8 pa0, bf16x8 pa1, bf16x8 pa2, bf16x8 pa3) {
;   const s16x4 l0 = tr_read<v_rd_off(D0, 0, 0)>(vb), h0 = tr_read<v_rd_off(D0, 0, 1)>(vb), l1 = tr_read<v_rd_off(D0, 1, 0)>(vb), h1 = tr_read<v_rd_off(D0, 1, 1)>(vb);
;   const s16x4 l2 = tr_read<v_rd_off(D0, 2, 0)>(vb), h2 = tr_read<v_rd_off(D0, 2, 1)>(vb), l3 = tr_read<v_rd_off(D0, 3, 0)>(vb), h3 = tr_read<v_rd_off(D0, 3, 1)>(vb);
;   asm volatile("s_waitcnt lgkmcnt(0)" ::: "memory"); SBAR();
;     ...
;   od = __builtin_amdgcn_mfma_f32_32x32x16_bf16(pa0, PK(l0, h0), od, 0, 0, 0);
;   od = __builtin_amdgcn_mfma_f32_32x32x16_bf16(pa1, PK(l1, h1), od, 0, 0, 0);
;   od = __builtin_amdgcn_mfma_f32_32x32x16_bf16(pa2, PK(l2, h2), od, 0, 0, 0);
;   od = __builtin_amdgcn_mfma_f32_32x32x16_bf16(pa3, PK(l3, h3), od, 0, 0, 0);
;     ...
; }
; __device__ __forceinline__ void pv_d0(f32x16* o, int vb, bf16x8 pa0, bf16x8 pa1, bf16x8 pa2, bf16x8 pa3) {
;   pv_one<0>(o[0], vb, pa0, pa1, pa2, pa3); pv_one<1>(o[1], vb, pa0, pa1, pa2, pa3); pv_one<2>(o[2], vb, pa0, pa1, pa2, pa3); pv_one<3>(o[3], vb, pa0, pa1, pa2, pa3);
	v_mfma_f32_32x32x16_bf16 v[32:47], v[146:149], v[204:207], v[32:47]
	ds_read_b64_tr_b16 v[204:205], v187 offset:0x600
	ds_read_b64_tr_b16 v[206:207], v187 offset:0xe00
	v_mfma_f32_32x32x16_bf16 v[32:47], v[200:203], v[208:211], v[32:47]
	ds_read_b64_tr_b16 v[208:209], v187 offset:0x1600
	ds_read_b64_tr_b16 v[210:211], v187 offset:0x1e00
	v_mfma_f32_32x32x16_bf16 v[32:47], v[152:155], v[212:215], v[32:47]
	ds_read_b64_tr_b16 v[212:213], v187 offset:0x2600
	ds_read_b64_tr_b16 v[214:215], v187 offset:0x2e00
	v_mfma_f32_32x32x16_bf16 v[32:47], v[156:159], v[222:225], v[32:47]
	ds_read_b64_tr_b16 v[222:223], v187 offset:0x3600
	ds_read_b64_tr_b16 v[224:225], v187 offset:0x3e00
	s_waitcnt lgkmcnt(0)
	v_mfma_f32_32x32x16_bf16 v[16:31], v[146:149], v[204:207], v[16:31]
	v_max_f32_e32 v146, v81, v81
	v_max_f32_e32 v147, v80, v80
	v_max_f32_e32 v146, v147, v146
	v_max3_f32 v146, v146, v82, v83
	v_max3_f32 v146, v146, v84, v85
	v_max3_f32 v146, v146, v86, v87
	v_max3_f32 v146, v146, v88, v89
	v_max3_f32 v146, v146, v90, v91
	v_max3_f32 v146, v146, v92, v93
	v_mfma_f32_32x32x16_bf16 v[16:31], v[200:203], v[208:211], v[16:31]
	v_max3_f32 v146, v146, v94, v95
	v_max3_f32 v146, v146, v64, v65
	v_max3_f32 v146, v146, v66, v67
	v_max3_f32 v146, v146, v68, v69
	v_max3_f32 v146, v146, v70, v71
	v_max3_f32 v146, v146, v72, v73
	v_max3_f32 v146, v146, v74, v75
	v_max3_f32 v146, v146, v76, v77
	v_mfma_f32_32x32x16_bf16 v[16:31], v[152:155], v[212:215], v[16:31]
	v_max3_f32 v146, v146, v78, v79
	v_mov_b32_e32 v147, v146
	s_nop 1
	v_permlane32_swap_b32_e32 v146, v147
	v_max_f32_e32 v147, v147, v147
	v_max_f32_e32 v146, v146, v146
	v_max_f32_e32 v146, v146, v147
	v_sub_f32_e32 v147, v146, v150
	v_cmp_ge_f32_e32 vcc, s87, v147
	v_max_f32_e32 v147, v150, v150
	v_max_f32_e32 v146, v147, v146
	v_mfma_f32_32x32x16_bf16 v[16:31], v[156:159], v[222:225], v[16:31]
	v_sub_f32_e32 v147, v150, v146
	v_mul_f32_e32 v147, 0x3e0293ee, v147
	v_exp_f32_e32 v147, v147
	s_cmp_eq_u64 vcc, exec
	s_cselect_b64 s[42:43], -1, 0
	s_waitcnt vmcnt(0)
	s_barrier
	v_cndmask_b32_e64 v200, v147, 1.0, s[42:43]
	v_cmp_gt_f32_e32 vcc, 1.0, v200
	s_cbranch_vccz .LBB0_458
	s_and_saveexec_b64 s[6:7], s[40:41]
	ds_write_b32 v184, v200 offset:128
	s_or_b64 exec, exec, s[6:7]
	s_waitcnt lgkmcnt(0)
	v_add_u32_e32 v147, v183, v96
	ds_read_b128 v[152:155], v147 offset:224
	ds_read_b128 v[156:159], v147 offset:192
	ds_read_b128 v[202:205], v147 offset:160
	ds_read_b128 v[206:209], v147 offset:128
	s_waitcnt lgkmcnt(3)
	v_pk_mul_f32 v[12:13], v[12:13], v[152:153]
	s_waitcnt lgkmcnt(2)
	v_pk_mul_f32 v[8:9], v[8:9], v[156:157]
	s_waitcnt lgkmcnt(1)
	v_pk_mul_f32 v[4:5], v[4:5], v[202:203]
	v_pk_mul_f32 v[14:15], v[14:15], v[154:155]
	v_pk_mul_f32 v[10:11], v[10:11], v[158:159]
	v_pk_mul_f32 v[6:7], v[6:7], v[204:205]
	s_waitcnt lgkmcnt(0)
	v_pk_mul_f32 v[2:3], v[2:3], v[208:209]
	v_pk_mul_f32 v[0:1], v[0:1], v[206:207]
	v_pk_mul_f32 v[60:61], v[60:61], v[152:153]
	v_pk_mul_f32 v[56:57], v[56:57], v[156:157]
	v_pk_mul_f32 v[52:53], v[52:53], v[202:203]
	v_pk_mul_f32 v[62:63], v[62:63], v[154:155]
	v_pk_mul_f32 v[58:59], v[58:59], v[158:159]
	v_pk_mul_f32 v[54:55], v[54:55], v[204:205]
	v_pk_mul_f32 v[50:51], v[50:51], v[208:209]
	v_pk_mul_f32 v[48:49], v[48:49], v[206:207]
	v_pk_mul_f32 v[44:45], v[44:45], v[152:153]
	v_pk_mul_f32 v[40:41], v[40:41], v[156:157]
	v_pk_mul_f32 v[36:37], v[36:37], v[202:203]
	v_pk_mul_f32 v[46:47], v[46:47], v[154:155]
	v_pk_mul_f32 v[42:43], v[42:43], v[158:159]
	v_pk_mul_f32 v[38:39], v[38:39], v[204:205]
	v_pk_mul_f32 v[34:35], v[34:35], v[208:209]
	v_pk_mul_f32 v[32:33], v[32:33], v[206:207]
	v_pk_mul_f32 v[28:29], v[28:29], v[152:153]
	v_pk_mul_f32 v[24:25], v[24:25], v[156:157]
	v_pk_mul_f32 v[20:21], v[20:21], v[202:203]
	v_pk_mul_f32 v[30:31], v[30:31], v[154:155]
	v_pk_mul_f32 v[26:27], v[26:27], v[158:159]
	v_pk_mul_f32 v[22:23], v[22:23], v[204:205]
	v_pk_mul_f32 v[18:19], v[18:19], v[208:209]
	v_pk_mul_f32 v[16:17], v[16:17], v[206:207]
; __device__ __forceinline__ void partialSM(f32x16& p0, f32x16& p1, float& m_reg, float& mn, float& alpha) {
;     ...
;   float mnC = -mn * C;
;   for (int r = 0; r < 16; ++r) p0[r] = fmaf(p0[r], C, mnC); for (int r = 0; r < 16; ++r) p1[r] = fmaf(p1[r], C, mnC);
;   for (int r = 0; r < 16; ++r) p0[r] = __builtin_amdgcn_exp2f(p0[r]);
; }
; __device__ __forceinline__ void finishSM(f32x16& p0, f32x16& p1, float alpha, float& l_reg, bf16x8& pa0, bf16x8& pa1, bf16x8& pa2, bf16x8& pa3) {
;   for (int r = 0; r < 16; ++r) p1[r] = __builtin_amdgcn_exp2f(p1[r]);
;   float ps = 0; for (int r = 0; r < 16; ++r) ps += p0[r]; for (int r = 0; r < 16; ++r) ps += p1[r];
;   { auto rr = __builtin_amdgcn_permlane32_swap(__float_as_uint(ps), __float_as_uint(ps), false, false);
;     ps = __uint_as_float(rr[0]) + __uint_as_float(rr[1]); }
;   l_reg = l_reg * alpha + ps;
;     ...
;   PK4(p0, 0, pa0); PK4(p0, 8, pa1); PK4(p1, 0, pa2); PK4(p1, 8, pa3);
;     ...
; }
; template <bool HALF> __device__ __forceinline__ void qkt(f32x16& p0, f32x16& p1, const char* Ks, const bf16x8* qr, int r32, int hi, int koff) {
;   p0 = f32x16{}; p1 = f32x16{};
;   for (int d0 = 0; d0 < (HALF ? 4 : 8); ++d0) { int cb = (d0 * 16 + hi * 8) * 2 + koff;
;     bf16x8 b0 = *reinterpret_cast<const bf16x8*>(Ks + KSWZ(r32, cb));
;     bf16x8 b1 = *reinterpret_cast<const bf16x8*>(Ks + KSWZ(32 + r32, cb));
;     p0 = __builtin_amdgcn_mfma_f32_32x32x16_bf16(b0, qr[d0], p0, 0, 0, 0);
;     p1 = __builtin_amdgcn_mfma_f32_32x32x16_bf16(b1, qr[d0], p1, 0, 0, 0); }
.LBB0_458:
	v_cndmask_b32_e64 v201, v146, v150, s[42:43]
	v_mul_f32_e32 v202, 0xbe0293ee, v201
	v_fmamk_f32 v80, v80, 0x3e0293ee, v202
	v_fmamk_f32 v81, v81, 0x3e0293ee, v202
	v_fmamk_f32 v82, v82, 0x3e0293ee, v202
	v_fmamk_f32 v83, v83, 0x3e0293ee, v202
	v_fmamk_f32 v84, v84, 0x3e0293ee, v202
	v_fmamk_f32 v85, v85, 0x3e0293ee, v202
	v_fmamk_f32 v86, v86, 0x3e0293ee, v202
	v_fmamk_f32 v87, v87, 0x3e0293ee, v202
	v_fmamk_f32 v88, v88, 0x3e0293ee, v202
	v_fmamk_f32 v89, v89, 0x3e0293ee, v202
	v_fmamk_f32 v90, v90, 0x3e0293ee, v202
	v_fmamk_f32 v91, v91, 0x3e0293ee, v202
	v_fmamk_f32 v92, v92, 0x3e0293ee, v202
	v_fmamk_f32 v93, v93, 0x3e0293ee, v202
	v_fmamk_f32 v94, v94, 0x3e0293ee, v202
	v_fmamk_f32 v95, v95, 0x3e0293ee, v202
	v_exp_f32_e32 v146, v80
	v_exp_f32_e32 v161, v81
	v_exp_f32_e32 v147, v82
	v_exp_f32_e32 v160, v83
	v_exp_f32_e32 v148, v84
	v_exp_f32_e32 v159, v85
	v_exp_f32_e32 v149, v86
	v_exp_f32_e32 v158, v87
	v_exp_f32_e32 v150, v88
	v_exp_f32_e32 v157, v89
	v_exp_f32_e32 v151, v90
	v_exp_f32_e32 v156, v91
	v_exp_f32_e32 v152, v92
	v_exp_f32_e32 v155, v93
	v_exp_f32_e32 v153, v94
	v_exp_f32_e32 v154, v95
	v_fmamk_f32 v211, v64, 0x3e0293ee, v202
	v_fmamk_f32 v221, v65, 0x3e0293ee, v202
	v_fmamk_f32 v222, v66, 0x3e0293ee, v202
	v_fmamk_f32 v223, v67, 0x3e0293ee, v202
	v_fmamk_f32 v224, v68, 0x3e0293ee, v202
	v_fmamk_f32 v204, v69, 0x3e0293ee, v202
	v_fmamk_f32 v205, v70, 0x3e0293ee, v202
	v_fmamk_f32 v206, v71, 0x3e0293ee, v202
	v_fmamk_f32 v207, v72, 0x3e0293ee, v202
	v_fmamk_f32 v208, v73, 0x3e0293ee, v202
	v_fmamk_f32 v209, v74, 0x3e0293ee, v202
	v_fmamk_f32 v210, v75, 0x3e0293ee, v202
	v_fmamk_f32 v203, v76, 0x3e0293ee, v202
	v_fmamk_f32 v225, v77, 0x3e0293ee, v202
	v_fmamk_f32 v226, v78, 0x3e0293ee, v202
	v_fmac_f32_e32 v202, 0x3e0293ee, v79
	s_waitcnt lgkmcnt(0)
	ds_read_b128 v[64:67], v192 offset:32768
	ds_read_b128 v[68:71], v192 offset:40960
	ds_read_b128 v[212:215], v193 offset:32768
	ds_read_b128 v[228:231], v193 offset:40960
	v_exp_f32_e32 v211, v211
	v_exp_f32_e32 v204, v204
	s_waitcnt lgkmcnt(3)
	v_mfma_f32_32x32x16_bf16 v[80:95], v[64:67], v[98:101], 0
	v_exp_f32_e32 v205, v205
	v_exp_f32_e32 v206, v206
	v_exp_f32_e32 v207, v207
	v_exp_f32_e32 v208, v208
	v_exp_f32_e32 v209, v209
	v_exp_f32_e32 v210, v210
	s_waitcnt lgkmcnt(2)
	v_mfma_f32_32x32x16_bf16 v[64:79], v[68:71], v[98:101], 0
	s_waitcnt lgkmcnt(1)
	v_mfma_f32_32x32x16_bf16 v[80:95], v[212:215], v[106:109], v[80:95]
	s_add_i32 m0, s52, 0x4000
	s_nop 0
	global_load_lds_dwordx4 v232, s[48:49]
	s_add_i32 m0, s52, 0x4400
	s_nop 0
	global_load_lds_dwordx4 v233, s[48:49]
	s_add_u32 s48, s48, 0x18000
	s_addc_u32 s49, s49, 0
	s_waitcnt lgkmcnt(0)
	v_mfma_f32_32x32x16_bf16 v[64:79], v[228:231], v[106:109], v[64:79]
	ds_read_b128 v[212:215], v195 offset:32768
	ds_read_b128 v[228:231], v195 offset:40960
	s_waitcnt lgkmcnt(1)
	v_mfma_f32_32x32x16_bf16 v[80:95], v[212:215], v[110:113], v[80:95]
	s_waitcnt lgkmcnt(0)
	v_mfma_f32_32x32x16_bf16 v[64:79], v[228:231], v[110:113], v[64:79]
	s_add_i32 m0, s53, 0x0
	s_nop 0
	global_load_lds_dwordx4 v234, s[50:51]
	s_add_i32 m0, s53, 0x400
	s_nop 0
	global_load_lds_dwordx4 v235, s[50:51]
	s_add_u32 s50, s50, 0xc0000
	s_addc_u32 s51, s51, 0
	ds_read_b128 v[212:215], v194 offset:32768
	ds_read_b128 v[228:231], v194 offset:40960
	s_waitcnt lgkmcnt(1)
	v_mfma_f32_32x32x16_bf16 v[80:95], v[212:215], v[102:105], v[80:95]
	v_exp_f32_e32 v215, v224
	v_exp_f32_e32 v224, v202
	v_add_f32_e32 v202, 0, v146
	v_add_f32_e32 v202, v161, v202
	v_add_f32_e32 v202, v147, v202
	v_add_f32_e32 v202, v160, v202
	v_add_f32_e32 v202, v148, v202
	v_add_f32_e32 v202, v159, v202
	v_add_f32_e32 v202, v149, v202
	v_add_f32_e32 v202, v158, v202
	v_add_f32_e32 v202, v150, v202
	v_add_f32_e32 v202, v157, v202
	v_add_f32_e32 v202, v151, v202
	v_add_f32_e32 v202, v156, v202
	v_add_f32_e32 v202, v152, v202
	v_exp_f32_e32 v212, v221
	v_add_f32_e32 v202, v155, v202
	v_exp_f32_e32 v213, v222
	v_add_f32_e32 v202, v153, v202
	v_exp_f32_e32 v214, v223
	v_add_f32_e32 v202, v154, v202
	v_add_f32_e32 v202, v211, v202
	v_add_f32_e32 v202, v212, v202
	v_add_f32_e32 v202, v213, v202
	v_add_f32_e32 v202, v214, v202
	v_add_f32_e32 v202, v215, v202
	v_add_f32_e32 v202, v204, v202
	v_add_f32_e32 v202, v205, v202
	v_add_f32_e32 v202, v206, v202
	v_exp_f32_e32 v221, v203
	v_add_f32_e32 v202, v207, v202
	v_exp_f32_e32 v222, v225
	v_add_f32_e32 v202, v208, v202
	s_waitcnt lgkmcnt(0)
	v_mfma_f32_32x32x16_bf16 v[64:79], v[228:231], v[102:105], v[64:79]
	v_exp_f32_e32 v223, v226
	v_add_f32_e32 v202, v209, v202
	v_add_f32_e32 v202, v210, v202
	v_add_f32_e32 v202, v221, v202
	v_add_f32_e32 v202, v222, v202
	v_add_f32_e32 v202, v223, v202
	v_add_f32_e32 v202, v224, v202
	v_mov_b32_e32 v203, v202
	v_cvt_pk_bf16_f32 v146, v146, v161
	v_cvt_pk_bf16_f32 v147, v147, v160
	v_cvt_pk_bf16_f32 v148, v148, v159
	v_cvt_pk_bf16_f32 v149, v149, v158
	v_cvt_pk_bf16_f32 v150, v150, v157
	v_cvt_pk_bf16_f32 v151, v151, v156
	v_cvt_pk_bf16_f32 v152, v152, v155
	v_cvt_pk_bf16_f32 v153, v153, v154
	v_cvt_pk_bf16_f32 v154, v211, v212
	v_cvt_pk_bf16_f32 v155, v213, v214
	v_cvt_pk_bf16_f32 v156, v215, v204
	v_cvt_pk_bf16_f32 v157, v205, v206
	v_cvt_pk_bf16_f32 v158, v207, v208
	v_cvt_pk_bf16_f32 v159, v209, v210
	v_cvt_pk_bf16_f32 v160, v221, v222
	v_cvt_pk_bf16_f32 v161, v223, v224
	s_nop 1
	v_permlane32_swap_b32_e32 v202, v203
	v_permlane32_swap_b32_e32 v146, v148
	v_permlane32_swap_b32_e32 v147, v149
	v_permlane32_swap_b32_e32 v150, v152
	v_permlane32_swap_b32_e32 v151, v153
	v_permlane32_swap_b32_e32 v154, v156
	v_permlane32_swap_b32_e32 v155, v157
	v_permlane32_swap_b32_e32 v158, v160
	v_permlane32_swap_b32_e32 v159, v161
	s_cmp_ge_u32 s3, s24
	s_cselect_b64 s[14:15], -1, 0
